# baseline (speedup 1.0000x reference)
.LBB1_52:
	ds_read_b128 v[138:141], v135
	ds_read_b128 v[142:145], v135 offset:1024
	ds_read_b128 v[146:149], v135 offset:2048
	ds_read_b128 v[150:153], v135 offset:3072
	ds_read_b128 v[154:157], v135 offset:4096
	ds_read_b128 v[158:161], v135 offset:5120
	s_add_u32 m0, s12, 0xc000
	ds_read_b128 v[162:165], v121
	ds_read_b128 v[182:185], v121 offset:1024
	ds_read_b128 v[186:189], v108
	global_load_lds_dwordx4 v236, s[8:9]
	s_add_u32 m0, s12, 0xe000
	ds_read_b128 v[190:193], v108 offset:1024
	global_load_lds_dwordx4 v237, s[8:9]
	s_waitcnt lgkmcnt(4)
	s_barrier
	s_waitcnt lgkmcnt(0)
	s_setprio 1
	s_waitcnt lgkmcnt(0)
	v_mfma_f32_16x16x32_f16 v[94:97], v[162:165], v[138:141], v[94:97]
	v_mfma_f32_16x16x32_f16 v[90:93], v[162:165], v[146:149], v[90:93]
	v_mfma_f32_16x16x32_f16 v[86:89], v[162:165], v[154:157], v[86:89]
	v_mfma_f32_16x16x32_f16 v[82:85], v[186:189], v[138:141], v[82:85]
	v_mfma_f32_16x16x32_f16 v[78:81], v[186:189], v[146:149], v[78:81]
	v_mfma_f32_16x16x32_f16 v[66:69], v[186:189], v[154:157], v[66:69]
	v_mfma_f32_16x16x32_f16 v[94:97], v[182:185], v[142:145], v[94:97]
	v_mfma_f32_16x16x32_f16 v[90:93], v[182:185], v[150:153], v[90:93]
	v_mfma_f32_16x16x32_f16 v[86:89], v[182:185], v[158:161], v[86:89]
	v_mfma_f32_16x16x32_f16 v[82:85], v[190:193], v[142:145], v[82:85]
	v_mfma_f32_16x16x32_f16 v[78:81], v[190:193], v[150:153], v[78:81]
	v_mfma_f32_16x16x32_f16 v[66:69], v[190:193], v[158:161], v[66:69]
	s_setprio 0
	s_barrier
	s_add_u32 m0, s12, 0x10000
	ds_read_b128 v[194:197], v134
	ds_read_b128 v[198:201], v134 offset:1024
	ds_read_b128 v[202:205], v134 offset:2048
	ds_read_b128 v[206:209], v134 offset:3072
	ds_read_b128 v[210:213], v134 offset:4096
	global_load_lds_dwordx4 v240, s[10:11]
	s_add_u32 m0, s12, 0x12000
	ds_read_b128 v[214:217], v134 offset:5120
	global_load_lds_dwordx4 v241, s[10:11]
	s_barrier
	s_waitcnt lgkmcnt(0)
	s_setprio 1
	s_waitcnt lgkmcnt(0)
	v_mfma_f32_16x16x32_f16 v[22:25], v[162:165], v[194:197], v[22:25]
	v_mfma_f32_16x16x32_f16 v[18:21], v[162:165], v[202:205], v[18:21]
	v_mfma_f32_16x16x32_f16 v[14:17], v[162:165], v[210:213], v[14:17]
	v_mfma_f32_16x16x32_f16 v[10:13], v[186:189], v[194:197], v[10:13]
	v_mfma_f32_16x16x32_f16 v[6:9], v[186:189], v[202:205], v[6:9]
	v_mfma_f32_16x16x32_f16 v[2:5], v[186:189], v[210:213], v[2:5]
	v_mfma_f32_16x16x32_f16 v[22:25], v[182:185], v[198:201], v[22:25]
	v_mfma_f32_16x16x32_f16 v[18:21], v[182:185], v[206:209], v[18:21]
	v_mfma_f32_16x16x32_f16 v[14:17], v[182:185], v[214:217], v[14:17]
	v_mfma_f32_16x16x32_f16 v[10:13], v[190:193], v[198:201], v[10:13]
	v_mfma_f32_16x16x32_f16 v[6:9], v[190:193], v[206:209], v[6:9]
	v_mfma_f32_16x16x32_f16 v[2:5], v[190:193], v[214:217], v[2:5]
	s_setprio 0
	s_add_u32 m0, s12, 0x0
	s_barrier
	ds_read_b128 v[162:165], v121 offset:16384
	ds_read_b128 v[182:185], v121 offset:17408
	ds_read_b128 v[186:189], v108 offset:16384
	global_load_lds_dwordx4 v232, s[8:9]
	s_add_u32 m0, s12, 0x2000
	ds_read_b128 v[190:193], v108 offset:17408
	global_load_lds_dwordx4 v233, s[8:9]
	s_barrier
	s_waitcnt lgkmcnt(0)
	s_setprio 1
	s_waitcnt lgkmcnt(0)
	v_mfma_f32_16x16x32_f16 v[26:29], v[162:165], v[138:141], v[26:29]
	v_mfma_f32_16x16x32_f16 v[30:33], v[162:165], v[146:149], v[30:33]
	v_mfma_f32_16x16x32_f16 v[34:37], v[162:165], v[154:157], v[34:37]
	v_mfma_f32_16x16x32_f16 v[38:41], v[186:189], v[138:141], v[38:41]
	v_mfma_f32_16x16x32_f16 v[46:49], v[186:189], v[146:149], v[46:49]
	v_mfma_f32_16x16x32_f16 v[54:57], v[186:189], v[154:157], v[54:57]
	v_mfma_f32_16x16x32_f16 v[26:29], v[182:185], v[142:145], v[26:29]
	v_mfma_f32_16x16x32_f16 v[30:33], v[182:185], v[150:153], v[30:33]
	v_mfma_f32_16x16x32_f16 v[34:37], v[182:185], v[158:161], v[34:37]
	v_mfma_f32_16x16x32_f16 v[38:41], v[190:193], v[142:145], v[38:41]
	v_mfma_f32_16x16x32_f16 v[46:49], v[190:193], v[150:153], v[46:49]
	v_mfma_f32_16x16x32_f16 v[54:57], v[190:193], v[158:161], v[54:57]
	s_setprio 0
	s_add_u32 m0, s12, 0x14000
	s_barrier
	global_load_lds_dwordx4 v244, s[10:11]
	s_add_u32 m0, s12, 0x16000
	s_nop 0
	global_load_lds_dwordx4 v245, s[10:11]
	s_waitcnt vmcnt(6)
	s_barrier
	s_setprio 1
	v_mfma_f32_16x16x32_f16 v[42:45], v[162:165], v[194:197], v[42:45]
	v_mfma_f32_16x16x32_f16 v[50:53], v[162:165], v[202:205], v[50:53]
	v_mfma_f32_16x16x32_f16 v[58:61], v[162:165], v[210:213], v[58:61]
	v_mfma_f32_16x16x32_f16 v[62:65], v[186:189], v[194:197], v[62:65]
	v_mfma_f32_16x16x32_f16 v[70:73], v[186:189], v[202:205], v[70:73]
	v_mfma_f32_16x16x32_f16 v[74:77], v[186:189], v[210:213], v[74:77]
	v_mfma_f32_16x16x32_f16 v[42:45], v[182:185], v[198:201], v[42:45]
	v_mfma_f32_16x16x32_f16 v[50:53], v[182:185], v[206:209], v[50:53]
	v_mfma_f32_16x16x32_f16 v[58:61], v[182:185], v[214:217], v[58:61]
	v_mfma_f32_16x16x32_f16 v[62:65], v[190:193], v[198:201], v[62:65]
	v_mfma_f32_16x16x32_f16 v[70:73], v[190:193], v[206:209], v[70:73]
	v_mfma_f32_16x16x32_f16 v[74:77], v[190:193], v[214:217], v[74:77]
	s_setprio 0
	s_barrier
	ds_read_b128 v[138:141], v127
	ds_read_b128 v[142:145], v127 offset:1024
	ds_read_b128 v[146:149], v127 offset:2048
	ds_read_b128 v[150:153], v127 offset:3072
	ds_read_b128 v[154:157], v127 offset:4096
	ds_read_b128 v[158:161], v127 offset:5120
	s_add_u32 m0, s12, 0x4000
	ds_read_b128 v[162:165], v121 offset:32768
	ds_read_b128 v[182:185], v121 offset:33792
	ds_read_b128 v[186:189], v108 offset:32768
	global_load_lds_dwordx4 v238, s[8:9]
	s_add_u32 m0, s12, 0x6000
	ds_read_b128 v[190:193], v108 offset:33792
	global_load_lds_dwordx4 v239, s[8:9]
	s_waitcnt lgkmcnt(4)
	s_barrier
	s_waitcnt lgkmcnt(0)
	s_setprio 1
	s_waitcnt lgkmcnt(0)
	v_mfma_f32_16x16x32_f16 v[94:97], v[162:165], v[138:141], v[94:97]
	v_mfma_f32_16x16x32_f16 v[90:93], v[162:165], v[146:149], v[90:93]
	v_mfma_f32_16x16x32_f16 v[86:89], v[162:165], v[154:157], v[86:89]
	v_mfma_f32_16x16x32_f16 v[82:85], v[186:189], v[138:141], v[82:85]
	v_mfma_f32_16x16x32_f16 v[78:81], v[186:189], v[146:149], v[78:81]
	v_mfma_f32_16x16x32_f16 v[66:69], v[186:189], v[154:157], v[66:69]
	v_mfma_f32_16x16x32_f16 v[94:97], v[182:185], v[142:145], v[94:97]
	v_mfma_f32_16x16x32_f16 v[90:93], v[182:185], v[150:153], v[90:93]
	v_mfma_f32_16x16x32_f16 v[86:89], v[182:185], v[158:161], v[86:89]
	v_mfma_f32_16x16x32_f16 v[82:85], v[190:193], v[142:145], v[82:85]
	v_mfma_f32_16x16x32_f16 v[78:81], v[190:193], v[150:153], v[78:81]
	v_mfma_f32_16x16x32_f16 v[66:69], v[190:193], v[158:161], v[66:69]
	s_setprio 0
	s_barrier
	s_add_u32 m0, s12, 0x18000
	ds_read_b128 v[194:197], v124
	ds_read_b128 v[198:201], v124 offset:1024
	ds_read_b128 v[202:205], v124 offset:2048
	ds_read_b128 v[206:209], v124 offset:3072
	ds_read_b128 v[210:213], v124 offset:4096
	global_load_lds_dwordx4 v242, s[10:11]
	s_add_u32 m0, s12, 0x1a000
	ds_read_b128 v[214:217], v124 offset:5120
	global_load_lds_dwordx4 v243, s[10:11]
	s_barrier
	s_waitcnt lgkmcnt(0)
	s_setprio 1
	s_waitcnt lgkmcnt(0)
	v_mfma_f32_16x16x32_f16 v[22:25], v[162:165], v[194:197], v[22:25]
	v_mfma_f32_16x16x32_f16 v[18:21], v[162:165], v[202:205], v[18:21]
	v_mfma_f32_16x16x32_f16 v[14:17], v[162:165], v[210:213], v[14:17]
	v_mfma_f32_16x16x32_f16 v[10:13], v[186:189], v[194:197], v[10:13]
	v_mfma_f32_16x16x32_f16 v[6:9], v[186:189], v[202:205], v[6:9]
	v_mfma_f32_16x16x32_f16 v[2:5], v[186:189], v[210:213], v[2:5]
	v_mfma_f32_16x16x32_f16 v[22:25], v[182:185], v[198:201], v[22:25]
	v_mfma_f32_16x16x32_f16 v[18:21], v[182:185], v[206:209], v[18:21]
	v_mfma_f32_16x16x32_f16 v[14:17], v[182:185], v[214:217], v[14:17]
	v_mfma_f32_16x16x32_f16 v[10:13], v[190:193], v[198:201], v[10:13]
	v_mfma_f32_16x16x32_f16 v[6:9], v[190:193], v[206:209], v[6:9]
	v_mfma_f32_16x16x32_f16 v[2:5], v[190:193], v[214:217], v[2:5]
	s_setprio 0
	s_add_u32 m0, s12, 0x8000
	s_barrier
	ds_read_b128 v[162:165], v121 offset:49152
	ds_read_b128 v[182:185], v121 offset:50176
	ds_read_b128 v[186:189], v108 offset:49152
	global_load_lds_dwordx4 v234, s[8:9]
	s_add_u32 m0, s12, 0xa000
	ds_read_b128 v[190:193], v108 offset:50176
	global_load_lds_dwordx4 v235, s[8:9]
	s_barrier
	s_waitcnt lgkmcnt(0)
	s_setprio 1
	s_waitcnt lgkmcnt(0)
	v_mfma_f32_16x16x32_f16 v[26:29], v[162:165], v[138:141], v[26:29]
	v_mfma_f32_16x16x32_f16 v[30:33], v[162:165], v[146:149], v[30:33]
	v_mfma_f32_16x16x32_f16 v[34:37], v[162:165], v[154:157], v[34:37]
	v_mfma_f32_16x16x32_f16 v[38:41], v[186:189], v[138:141], v[38:41]
	v_mfma_f32_16x16x32_f16 v[46:49], v[186:189], v[146:149], v[46:49]
	v_mfma_f32_16x16x32_f16 v[54:57], v[186:189], v[154:157], v[54:57]
	v_mfma_f32_16x16x32_f16 v[26:29], v[182:185], v[142:145], v[26:29]
	v_mfma_f32_16x16x32_f16 v[30:33], v[182:185], v[150:153], v[30:33]
	v_mfma_f32_16x16x32_f16 v[34:37], v[182:185], v[158:161], v[34:37]
	v_mfma_f32_16x16x32_f16 v[38:41], v[190:193], v[142:145], v[38:41]
	v_mfma_f32_16x16x32_f16 v[46:49], v[190:193], v[150:153], v[46:49]
	v_mfma_f32_16x16x32_f16 v[54:57], v[190:193], v[158:161], v[54:57]
	s_setprio 0
	s_add_u32 m0, s12, 0x1c000
	s_barrier
	global_load_lds_dwordx4 v246, s[10:11]
	s_add_u32 m0, s12, 0x1e000
	s_nop 0
	global_load_lds_dwordx4 v247, s[10:11]
	s_waitcnt vmcnt(6)
	s_barrier
	s_setprio 1
	v_mfma_f32_16x16x32_f16 v[42:45], v[162:165], v[194:197], v[42:45]
	v_mfma_f32_16x16x32_f16 v[50:53], v[162:165], v[202:205], v[50:53]
	v_mfma_f32_16x16x32_f16 v[58:61], v[162:165], v[210:213], v[58:61]
	v_mfma_f32_16x16x32_f16 v[62:65], v[186:189], v[194:197], v[62:65]
	v_mfma_f32_16x16x32_f16 v[70:73], v[186:189], v[202:205], v[70:73]
	v_mfma_f32_16x16x32_f16 v[74:77], v[186:189], v[210:213], v[74:77]
	v_mfma_f32_16x16x32_f16 v[42:45], v[182:185], v[198:201], v[42:45]
	v_mfma_f32_16x16x32_f16 v[50:53], v[182:185], v[206:209], v[50:53]
	v_mfma_f32_16x16x32_f16 v[58:61], v[182:185], v[214:217], v[58:61]
	v_mfma_f32_16x16x32_f16 v[62:65], v[190:193], v[198:201], v[62:65]
	v_mfma_f32_16x16x32_f16 v[70:73], v[190:193], v[206:209], v[70:73]
	v_mfma_f32_16x16x32_f16 v[74:77], v[190:193], v[214:217], v[74:77]
	s_setprio 0
	s_add_i32 s4, s4, 2
	s_add_u32 s2, s2, 0x100
	s_addc_u32 s3, s3, 0
	s_add_u32 s8, s8, 0x100
	s_addc_u32 s9, s9, 0
	s_add_u32 s10, s10, 0x100
	s_addc_u32 s11, s11, 0
	s_cmp_lt_u32 s4, 8
	s_barrier
	s_cbranch_scc1 .LBB1_52
	s_mov_b64 s[4:5], 0x580
	v_readfirstlane_b32 s2, v136
	v_lshl_add_u64 v[98:99], v[98:99], 0, s[4:5]
	s_mov_b32 m0, s2
	v_readfirstlane_b32 s2, v137
	ds_read_b128 v[102:105], v135
	ds_read_b128 v[110:113], v135 offset:1024
	ds_read_b128 v[114:117], v135 offset:2048
	ds_read_b128 v[128:131], v135 offset:3072
	ds_read_b128 v[138:141], v135 offset:4096
	ds_read_b128 v[142:145], v135 offset:5120
	ds_read_b128 v[146:149], v121
	ds_read_b128 v[150:153], v121 offset:1024
	ds_read_b128 v[154:157], v108
	ds_read_b128 v[158:161], v108 offset:1024
	global_load_lds_dwordx4 v[98:99], off
	v_lshl_add_u64 v[98:99], v[100:101], 0, s[4:5]
	s_mov_b32 m0, s2
	s_nop 0
	global_load_lds_dwordx4 v[98:99], off
	s_barrier
	s_waitcnt lgkmcnt(0)
	s_setprio 1
	s_waitcnt lgkmcnt(0)
	v_mfma_f32_16x16x32_f16 v[94:97], v[146:149], v[102:105], v[94:97]
	v_mfma_f32_16x16x32_f16 v[90:93], v[146:149], v[114:117], v[90:93]
	v_mfma_f32_16x16x32_f16 v[86:89], v[146:149], v[138:141], v[86:89]
	v_mfma_f32_16x16x32_f16 v[82:85], v[154:157], v[102:105], v[82:85]
	v_mfma_f32_16x16x32_f16 v[78:81], v[154:157], v[114:117], v[78:81]
	v_mfma_f32_16x16x32_f16 v[66:69], v[154:157], v[138:141], v[66:69]
	v_mfma_f32_16x16x32_f16 v[94:97], v[150:153], v[110:113], v[94:97]
	v_mfma_f32_16x16x32_f16 v[90:93], v[150:153], v[128:131], v[90:93]
	v_mfma_f32_16x16x32_f16 v[86:89], v[150:153], v[142:145], v[86:89]
	v_mfma_f32_16x16x32_f16 v[82:85], v[158:161], v[110:113], v[82:85]
	v_mfma_f32_16x16x32_f16 v[98:101], v[158:161], v[128:131], v[78:81]
	v_mfma_f32_16x16x32_f16 v[66:69], v[158:161], v[142:145], v[66:69]
	s_setprio 0
	s_barrier
	ds_read_b128 v[78:81], v134
	ds_read_b128 v[162:165], v134 offset:1024
	ds_read_b128 v[182:185], v134 offset:2048
	ds_read_b128 v[186:189], v134 offset:3072
	ds_read_b128 v[190:193], v134 offset:4096
	ds_read_b128 v[132:135], v134 offset:5120
	s_barrier
	s_waitcnt lgkmcnt(0)
	s_setprio 1
	s_waitcnt lgkmcnt(0)
	v_mfma_f32_16x16x32_f16 v[22:25], v[146:149], v[78:81], v[22:25]
	v_mfma_f32_16x16x32_f16 v[18:21], v[146:149], v[182:185], v[18:21]
	v_mfma_f32_16x16x32_f16 v[14:17], v[146:149], v[190:193], v[14:17]
	v_mfma_f32_16x16x32_f16 v[10:13], v[154:157], v[78:81], v[10:13]
	v_mfma_f32_16x16x32_f16 v[6:9], v[154:157], v[182:185], v[6:9]
	v_mfma_f32_16x16x32_f16 v[2:5], v[154:157], v[190:193], v[2:5]
	v_mfma_f32_16x16x32_f16 v[22:25], v[150:153], v[162:165], v[22:25]
	v_mfma_f32_16x16x32_f16 v[18:21], v[150:153], v[186:189], v[18:21]
	v_mfma_f32_16x16x32_f16 v[14:17], v[150:153], v[132:135], v[14:17]
	v_mfma_f32_16x16x32_f16 v[10:13], v[158:161], v[162:165], v[10:13]
	v_mfma_f32_16x16x32_f16 v[6:9], v[158:161], v[186:189], v[6:9]
	v_mfma_f32_16x16x32_f16 v[2:5], v[158:161], v[132:135], v[2:5]
	s_setprio 0
	s_barrier
	ds_read_b128 v[146:149], v121 offset:16384
	ds_read_b128 v[150:153], v121 offset:17408
	ds_read_b128 v[154:157], v108 offset:16384
	ds_read_b128 v[158:161], v108 offset:17408
	s_waitcnt vmcnt(4)
	s_barrier
	s_waitcnt lgkmcnt(0)
	s_setprio 1
	s_waitcnt lgkmcnt(0)
	v_mfma_f32_16x16x32_f16 v[26:29], v[146:149], v[102:105], v[26:29]
	v_mfma_f32_16x16x32_f16 v[30:33], v[146:149], v[114:117], v[30:33]
	v_mfma_f32_16x16x32_f16 v[34:37], v[146:149], v[138:141], v[34:37]
	v_mfma_f32_16x16x32_f16 v[38:41], v[154:157], v[102:105], v[38:41]
	v_mfma_f32_16x16x32_f16 v[46:49], v[154:157], v[114:117], v[46:49]
	v_mfma_f32_16x16x32_f16 v[26:29], v[150:153], v[110:113], v[26:29]
	v_mfma_f32_16x16x32_f16 v[30:33], v[150:153], v[128:131], v[30:33]
	v_mfma_f32_16x16x32_f16 v[34:37], v[150:153], v[142:145], v[34:37]
	v_mfma_f32_16x16x32_f16 v[38:41], v[158:161], v[110:113], v[38:41]
	v_mfma_f32_16x16x32_f16 v[46:49], v[158:161], v[128:131], v[46:49]
	v_mfma_f32_16x16x32_f16 v[54:57], v[154:157], v[138:141], v[54:57]
	v_mfma_f32_16x16x32_f16 v[54:57], v[158:161], v[142:145], v[54:57]
	s_setprio 0
	s_setprio 1
	v_mfma_f32_16x16x32_f16 v[58:61], v[146:149], v[190:193], v[58:61]
	v_mfma_f32_16x16x32_f16 v[110:113], v[150:153], v[132:135], v[58:61]
	v_mfma_f32_16x16x32_f16 v[58:61], v[154:157], v[78:81], v[62:65]
	v_mfma_f32_16x16x32_f16 v[42:45], v[146:149], v[78:81], v[42:45]
	v_mfma_f32_16x16x32_f16 v[114:117], v[158:161], v[162:165], v[58:61]
	v_mfma_f32_16x16x32_f16 v[58:61], v[154:157], v[182:185], v[70:73]
	v_mfma_f32_16x16x32_f16 v[42:45], v[150:153], v[162:165], v[42:45]
	v_mfma_f32_16x16x32_f16 v[50:53], v[146:149], v[182:185], v[50:53]
	v_mfma_f32_16x16x32_f16 v[128:131], v[158:161], v[186:189], v[58:61]
	v_mfma_f32_16x16x32_f16 v[58:61], v[154:157], v[190:193], v[74:77]
	v_mfma_f32_16x16x32_f16 v[50:53], v[150:153], v[186:189], v[50:53]
	v_mfma_f32_16x16x32_f16 v[132:135], v[158:161], v[132:135], v[58:61]
	s_setprio 0
	s_barrier
	ds_read_b128 v[136:139], v127
	ds_read_b128 v[140:143], v127 offset:1024
	ds_read_b128 v[144:147], v127 offset:2048
	ds_read_b128 v[148:151], v127 offset:3072
	ds_read_b128 v[152:155], v127 offset:4096
	ds_read_b128 v[156:159], v127 offset:5120
	ds_read_b128 v[74:77], v121 offset:32768
	ds_read_b128 v[160:163], v121 offset:33792
	ds_read_b128 v[164:167], v108 offset:32768
	ds_read_b128 v[182:185], v108 offset:33792
	s_waitcnt vmcnt(2)
	s_barrier
	s_waitcnt lgkmcnt(0)
	s_setprio 1
	s_waitcnt lgkmcnt(0)
	v_mfma_f32_16x16x32_f16 v[62:65], v[74:77], v[144:147], v[90:93]
	v_mfma_f32_16x16x32_f16 v[70:73], v[164:167], v[136:139], v[82:85]
	v_mfma_f32_16x16x32_f16 v[58:61], v[74:77], v[136:139], v[94:97]
	v_mfma_f32_16x16x32_f16 v[78:81], v[160:163], v[148:151], v[62:65]
	v_mfma_f32_16x16x32_f16 v[62:65], v[74:77], v[152:155], v[86:89]
	v_mfma_f32_16x16x32_f16 v[102:105], v[182:185], v[140:143], v[70:73]
	v_mfma_f32_16x16x32_f16 v[70:73], v[164:167], v[144:147], v[98:101]
	v_mfma_f32_16x16x32_f16 v[66:69], v[164:167], v[152:155], v[66:69]
	v_mfma_f32_16x16x32_f16 v[58:61], v[160:163], v[140:143], v[58:61]
	v_mfma_f32_16x16x32_f16 v[62:65], v[160:163], v[156:159], v[62:65]
	v_mfma_f32_16x16x32_f16 v[86:89], v[182:185], v[148:151], v[70:73]
	v_mfma_f32_16x16x32_f16 v[70:73], v[182:185], v[156:159], v[66:69]
	s_setprio 0
	s_barrier
	ds_read_b128 v[186:189], v124
	ds_read_b128 v[190:193], v124 offset:1024
	ds_read_b128 v[194:197], v124 offset:2048
	ds_read_b128 v[198:201], v124 offset:3072
	ds_read_b128 v[202:205], v124 offset:4096
	ds_read_b128 v[122:125], v124 offset:5120
	s_waitcnt vmcnt(0)
	s_barrier
	s_waitcnt lgkmcnt(0)
	s_setprio 1
	s_waitcnt lgkmcnt(0)
	v_mfma_f32_16x16x32_f16 v[22:25], v[74:77], v[186:189], v[22:25]
	v_mfma_f32_16x16x32_f16 v[18:21], v[74:77], v[194:197], v[18:21]
	v_mfma_f32_16x16x32_f16 v[14:17], v[74:77], v[202:205], v[14:17]
	v_mfma_f32_16x16x32_f16 v[10:13], v[164:167], v[186:189], v[10:13]
	v_mfma_f32_16x16x32_f16 v[6:9], v[164:167], v[194:197], v[6:9]
	v_mfma_f32_16x16x32_f16 v[2:5], v[164:167], v[202:205], v[2:5]
	v_mfma_f32_16x16x32_f16 v[94:97], v[160:163], v[190:193], v[22:25]
	v_mfma_f32_16x16x32_f16 v[82:85], v[160:163], v[198:201], v[18:21]
	v_mfma_f32_16x16x32_f16 v[66:69], v[160:163], v[122:125], v[14:17]
	v_mfma_f32_16x16x32_f16 v[98:101], v[182:185], v[190:193], v[10:13]
	v_mfma_f32_16x16x32_f16 v[90:93], v[182:185], v[198:201], v[6:9]
	v_mfma_f32_16x16x32_f16 v[74:77], v[182:185], v[122:125], v[2:5]
	s_setprio 0
	s_barrier
	ds_read_b128 v[10:13], v121 offset:49152
	ds_read_b128 v[160:163], v121 offset:50176
	ds_read_b128 v[164:167], v108 offset:49152
	ds_read_b128 v[182:185], v108 offset:50176
	s_barrier
	s_waitcnt lgkmcnt(0)
	s_setprio 1
	s_waitcnt lgkmcnt(0)
	v_mfma_f32_16x16x32_f16 v[2:5], v[10:13], v[136:139], v[26:29]
	v_mfma_f32_16x16x32_f16 v[18:21], v[164:167], v[136:139], v[38:41]
	v_mfma_f32_16x16x32_f16 v[14:17], v[160:163], v[140:143], v[2:5]
	v_mfma_f32_16x16x32_f16 v[2:5], v[10:13], v[144:147], v[30:33]
	v_mfma_f32_16x16x32_f16 v[38:41], v[182:185], v[140:143], v[18:21]
	v_mfma_f32_16x16x32_f16 v[18:21], v[164:167], v[144:147], v[46:49]
	v_mfma_f32_16x16x32_f16 v[6:9], v[160:163], v[148:151], v[2:5]
	v_mfma_f32_16x16x32_f16 v[2:5], v[10:13], v[152:155], v[34:37]
	v_mfma_f32_16x16x32_f16 v[26:29], v[182:185], v[148:151], v[18:21]
	v_mfma_f32_16x16x32_f16 v[18:21], v[164:167], v[152:155], v[54:57]
	v_mfma_f32_16x16x32_f16 v[2:5], v[160:163], v[156:159], v[2:5]
	v_mfma_f32_16x16x32_f16 v[18:21], v[182:185], v[156:159], v[18:21]
	s_setprio 0
	s_setprio 1
	v_mfma_f32_16x16x32_f16 v[34:37], v[164:167], v[186:189], v[114:117]
	v_mfma_f32_16x16x32_f16 v[22:25], v[10:13], v[186:189], v[42:45]
	v_mfma_f32_16x16x32_f16 v[46:49], v[182:185], v[190:193], v[34:37]
	v_mfma_f32_16x16x32_f16 v[34:37], v[164:167], v[194:197], v[128:131]
	v_mfma_f32_16x16x32_f16 v[30:33], v[160:163], v[190:193], v[22:25]
	v_mfma_f32_16x16x32_f16 v[22:25], v[10:13], v[194:197], v[50:53]
	v_mfma_f32_16x16x32_f16 v[10:13], v[10:13], v[202:205], v[110:113]
	v_mfma_f32_16x16x32_f16 v[42:45], v[182:185], v[198:201], v[34:37]
	v_mfma_f32_16x16x32_f16 v[34:37], v[164:167], v[202:205], v[132:135]
	v_mfma_f32_16x16x32_f16 v[22:25], v[160:163], v[198:201], v[22:25]
	v_mfma_f32_16x16x32_f16 v[10:13], v[160:163], v[122:125], v[10:13]
	v_mfma_f32_16x16x32_f16 v[34:37], v[182:185], v[122:125], v[34:37]
	s_setprio 0
	s_movk_i32 s2, 0x100
	v_cmp_gt_u32_e32 vcc, s2, v175
	s_barrier
	s_and_saveexec_b64 s[2:3], vcc
	s_cbranch_execz .LBB1_55
	s_barrier

.LBB1_66:
	ds_read_b128 v[148:151], v144
	ds_read_b128 v[152:155], v144 offset:1024
	ds_read_b128 v[156:159], v144 offset:2048
	ds_read_b128 v[160:163], v144 offset:3072
	ds_read_b128 v[164:167], v144 offset:4096
	ds_read_b128 v[174:177], v144 offset:5120
	s_add_u32 m0, s12, 0xc000
	ds_read_b128 v[178:181], v130
	ds_read_b128 v[182:185], v130 offset:1024
	ds_read_b128 v[186:189], v108
	global_load_lds_dwordx4 v236, s[8:9]
	s_add_u32 m0, s12, 0xe000
	ds_read_b128 v[190:193], v108 offset:1024
	global_load_lds_dwordx4 v237, s[8:9]
	s_waitcnt lgkmcnt(4)
	s_barrier
	s_waitcnt lgkmcnt(0)
	s_setprio 1
	s_waitcnt lgkmcnt(0)
	v_mfma_f32_16x16x32_f16 v[94:97], v[178:181], v[148:151], v[94:97]
	v_mfma_f32_16x16x32_f16 v[90:93], v[178:181], v[156:159], v[90:93]
	v_mfma_f32_16x16x32_f16 v[86:89], v[178:181], v[164:167], v[86:89]
	v_mfma_f32_16x16x32_f16 v[74:77], v[186:189], v[148:151], v[74:77]
	v_mfma_f32_16x16x32_f16 v[46:49], v[186:189], v[156:159], v[46:49]
	v_mfma_f32_16x16x32_f16 v[18:21], v[186:189], v[164:167], v[18:21]
	v_mfma_f32_16x16x32_f16 v[94:97], v[182:185], v[152:155], v[94:97]
	v_mfma_f32_16x16x32_f16 v[90:93], v[182:185], v[160:163], v[90:93]
	v_mfma_f32_16x16x32_f16 v[86:89], v[182:185], v[174:177], v[86:89]
	v_mfma_f32_16x16x32_f16 v[74:77], v[190:193], v[152:155], v[74:77]
	v_mfma_f32_16x16x32_f16 v[46:49], v[190:193], v[160:163], v[46:49]
	v_mfma_f32_16x16x32_f16 v[18:21], v[190:193], v[174:177], v[18:21]
	s_setprio 0
	s_barrier
	s_add_u32 m0, s12, 0x10000
	ds_read_b128 v[194:197], v143
	ds_read_b128 v[198:201], v143 offset:1024
	ds_read_b128 v[202:205], v143 offset:2048
	ds_read_b128 v[206:209], v143 offset:3072
	ds_read_b128 v[210:213], v143 offset:4096
	global_load_lds_dwordx4 v240, s[10:11]
	s_add_u32 m0, s12, 0x12000
	ds_read_b128 v[214:217], v143 offset:5120
	global_load_lds_dwordx4 v241, s[10:11]
	s_barrier
	s_waitcnt lgkmcnt(0)
	s_setprio 1
	s_waitcnt lgkmcnt(0)
	v_mfma_f32_16x16x32_f16 v[10:13], v[178:181], v[194:197], v[10:13]
	v_mfma_f32_16x16x32_f16 v[6:9], v[178:181], v[202:205], v[6:9]
	v_mfma_f32_16x16x32_f16 v[2:5], v[178:181], v[210:213], v[2:5]
	v_mfma_f32_16x16x32_f16 v[26:29], v[186:189], v[194:197], v[26:29]
	v_mfma_f32_16x16x32_f16 v[34:37], v[186:189], v[202:205], v[34:37]
	v_mfma_f32_16x16x32_f16 v[50:53], v[186:189], v[210:213], v[50:53]
	v_mfma_f32_16x16x32_f16 v[10:13], v[182:185], v[198:201], v[10:13]
	v_mfma_f32_16x16x32_f16 v[6:9], v[182:185], v[206:209], v[6:9]
	v_mfma_f32_16x16x32_f16 v[2:5], v[182:185], v[214:217], v[2:5]
	v_mfma_f32_16x16x32_f16 v[26:29], v[190:193], v[198:201], v[26:29]
	v_mfma_f32_16x16x32_f16 v[34:37], v[190:193], v[206:209], v[34:37]
	v_mfma_f32_16x16x32_f16 v[50:53], v[190:193], v[214:217], v[50:53]
	s_setprio 0
	s_add_u32 m0, s12, 0x0
	s_barrier
	ds_read_b128 v[178:181], v130 offset:16384
	ds_read_b128 v[182:185], v130 offset:17408
	ds_read_b128 v[186:189], v108 offset:16384
	global_load_lds_dwordx4 v232, s[8:9]
	s_add_u32 m0, s12, 0x2000
	ds_read_b128 v[190:193], v108 offset:17408
	global_load_lds_dwordx4 v233, s[8:9]
	s_barrier
	s_waitcnt lgkmcnt(0)
	s_setprio 1
	s_waitcnt lgkmcnt(0)
	v_mfma_f32_16x16x32_f16 v[14:17], v[178:181], v[148:151], v[14:17]
	v_mfma_f32_16x16x32_f16 v[22:25], v[178:181], v[156:159], v[22:25]
	v_mfma_f32_16x16x32_f16 v[30:33], v[178:181], v[164:167], v[30:33]
	v_mfma_f32_16x16x32_f16 v[38:41], v[186:189], v[148:151], v[38:41]
	v_mfma_f32_16x16x32_f16 v[54:57], v[186:189], v[156:159], v[54:57]
	v_mfma_f32_16x16x32_f16 v[62:65], v[186:189], v[164:167], v[62:65]
	v_mfma_f32_16x16x32_f16 v[14:17], v[182:185], v[152:155], v[14:17]
	v_mfma_f32_16x16x32_f16 v[22:25], v[182:185], v[160:163], v[22:25]
	v_mfma_f32_16x16x32_f16 v[30:33], v[182:185], v[174:177], v[30:33]
	v_mfma_f32_16x16x32_f16 v[38:41], v[190:193], v[152:155], v[38:41]
	v_mfma_f32_16x16x32_f16 v[54:57], v[190:193], v[160:163], v[54:57]
	v_mfma_f32_16x16x32_f16 v[62:65], v[190:193], v[174:177], v[62:65]
	s_setprio 0
	s_add_u32 m0, s12, 0x14000
	s_barrier
	global_load_lds_dwordx4 v244, s[10:11]
	s_add_u32 m0, s12, 0x16000
	s_nop 0
	global_load_lds_dwordx4 v245, s[10:11]
	s_waitcnt vmcnt(6)
	s_barrier
	s_setprio 1
	v_mfma_f32_16x16x32_f16 v[42:45], v[178:181], v[194:197], v[42:45]
	v_mfma_f32_16x16x32_f16 v[58:61], v[178:181], v[202:205], v[58:61]
	v_mfma_f32_16x16x32_f16 v[66:69], v[178:181], v[210:213], v[66:69]
	v_mfma_f32_16x16x32_f16 v[70:73], v[186:189], v[194:197], v[70:73]
	v_mfma_f32_16x16x32_f16 v[78:81], v[186:189], v[202:205], v[78:81]
	v_mfma_f32_16x16x32_f16 v[82:85], v[186:189], v[210:213], v[82:85]
	v_mfma_f32_16x16x32_f16 v[42:45], v[182:185], v[198:201], v[42:45]
	v_mfma_f32_16x16x32_f16 v[58:61], v[182:185], v[206:209], v[58:61]
	v_mfma_f32_16x16x32_f16 v[66:69], v[182:185], v[214:217], v[66:69]
	v_mfma_f32_16x16x32_f16 v[70:73], v[190:193], v[198:201], v[70:73]
	v_mfma_f32_16x16x32_f16 v[78:81], v[190:193], v[206:209], v[78:81]
	v_mfma_f32_16x16x32_f16 v[82:85], v[190:193], v[214:217], v[82:85]
	s_setprio 0
	s_barrier
	ds_read_b128 v[148:151], v136
	ds_read_b128 v[152:155], v136 offset:1024
	ds_read_b128 v[156:159], v136 offset:2048
	ds_read_b128 v[160:163], v136 offset:3072
	ds_read_b128 v[164:167], v136 offset:4096
	ds_read_b128 v[174:177], v136 offset:5120
	s_add_u32 m0, s12, 0x4000
	ds_read_b128 v[178:181], v130 offset:32768
	ds_read_b128 v[182:185], v130 offset:33792
	ds_read_b128 v[186:189], v108 offset:32768
	global_load_lds_dwordx4 v238, s[8:9]
	s_add_u32 m0, s12, 0x6000
	ds_read_b128 v[190:193], v108 offset:33792
	global_load_lds_dwordx4 v239, s[8:9]
	s_waitcnt lgkmcnt(4)
	s_barrier
	s_waitcnt lgkmcnt(0)
	s_setprio 1
	s_waitcnt lgkmcnt(0)
	v_mfma_f32_16x16x32_f16 v[94:97], v[178:181], v[148:151], v[94:97]
	v_mfma_f32_16x16x32_f16 v[90:93], v[178:181], v[156:159], v[90:93]
	v_mfma_f32_16x16x32_f16 v[86:89], v[178:181], v[164:167], v[86:89]
	v_mfma_f32_16x16x32_f16 v[74:77], v[186:189], v[148:151], v[74:77]
	v_mfma_f32_16x16x32_f16 v[46:49], v[186:189], v[156:159], v[46:49]
	v_mfma_f32_16x16x32_f16 v[18:21], v[186:189], v[164:167], v[18:21]
	v_mfma_f32_16x16x32_f16 v[94:97], v[182:185], v[152:155], v[94:97]
	v_mfma_f32_16x16x32_f16 v[90:93], v[182:185], v[160:163], v[90:93]
	v_mfma_f32_16x16x32_f16 v[86:89], v[182:185], v[174:177], v[86:89]
	v_mfma_f32_16x16x32_f16 v[74:77], v[190:193], v[152:155], v[74:77]
	v_mfma_f32_16x16x32_f16 v[46:49], v[190:193], v[160:163], v[46:49]
	v_mfma_f32_16x16x32_f16 v[18:21], v[190:193], v[174:177], v[18:21]
	s_setprio 0
	s_barrier
	s_add_u32 m0, s12, 0x18000
	ds_read_b128 v[194:197], v133
	ds_read_b128 v[198:201], v133 offset:1024
	ds_read_b128 v[202:205], v133 offset:2048
	ds_read_b128 v[206:209], v133 offset:3072
	ds_read_b128 v[210:213], v133 offset:4096
	global_load_lds_dwordx4 v242, s[10:11]
	s_add_u32 m0, s12, 0x1a000
	ds_read_b128 v[214:217], v133 offset:5120
	global_load_lds_dwordx4 v243, s[10:11]
	s_barrier
	s_waitcnt lgkmcnt(0)
	s_setprio 1
	s_waitcnt lgkmcnt(0)
	v_mfma_f32_16x16x32_f16 v[10:13], v[178:181], v[194:197], v[10:13]
	v_mfma_f32_16x16x32_f16 v[6:9], v[178:181], v[202:205], v[6:9]
	v_mfma_f32_16x16x32_f16 v[2:5], v[178:181], v[210:213], v[2:5]
	v_mfma_f32_16x16x32_f16 v[26:29], v[186:189], v[194:197], v[26:29]
	v_mfma_f32_16x16x32_f16 v[34:37], v[186:189], v[202:205], v[34:37]
	v_mfma_f32_16x16x32_f16 v[50:53], v[186:189], v[210:213], v[50:53]
	v_mfma_f32_16x16x32_f16 v[10:13], v[182:185], v[198:201], v[10:13]
	v_mfma_f32_16x16x32_f16 v[6:9], v[182:185], v[206:209], v[6:9]
	v_mfma_f32_16x16x32_f16 v[2:5], v[182:185], v[214:217], v[2:5]
	v_mfma_f32_16x16x32_f16 v[26:29], v[190:193], v[198:201], v[26:29]
	v_mfma_f32_16x16x32_f16 v[34:37], v[190:193], v[206:209], v[34:37]
	v_mfma_f32_16x16x32_f16 v[50:53], v[190:193], v[214:217], v[50:53]
	s_setprio 0
	s_add_u32 m0, s12, 0x8000
	s_barrier
	ds_read_b128 v[178:181], v130 offset:49152
	ds_read_b128 v[182:185], v130 offset:50176
	ds_read_b128 v[186:189], v108 offset:49152
	global_load_lds_dwordx4 v234, s[8:9]
	s_add_u32 m0, s12, 0xa000
	ds_read_b128 v[190:193], v108 offset:50176
	global_load_lds_dwordx4 v235, s[8:9]
	s_barrier
	s_waitcnt lgkmcnt(0)
	s_setprio 1
	s_waitcnt lgkmcnt(0)
	v_mfma_f32_16x16x32_f16 v[14:17], v[178:181], v[148:151], v[14:17]
	v_mfma_f32_16x16x32_f16 v[22:25], v[178:181], v[156:159], v[22:25]
	v_mfma_f32_16x16x32_f16 v[30:33], v[178:181], v[164:167], v[30:33]
	v_mfma_f32_16x16x32_f16 v[38:41], v[186:189], v[148:151], v[38:41]
	v_mfma_f32_16x16x32_f16 v[54:57], v[186:189], v[156:159], v[54:57]
	v_mfma_f32_16x16x32_f16 v[62:65], v[186:189], v[164:167], v[62:65]
	v_mfma_f32_16x16x32_f16 v[14:17], v[182:185], v[152:155], v[14:17]
	v_mfma_f32_16x16x32_f16 v[22:25], v[182:185], v[160:163], v[22:25]
	v_mfma_f32_16x16x32_f16 v[30:33], v[182:185], v[174:177], v[30:33]
	v_mfma_f32_16x16x32_f16 v[38:41], v[190:193], v[152:155], v[38:41]
	v_mfma_f32_16x16x32_f16 v[54:57], v[190:193], v[160:163], v[54:57]
	v_mfma_f32_16x16x32_f16 v[62:65], v[190:193], v[174:177], v[62:65]
	s_setprio 0
	s_add_u32 m0, s12, 0x1c000
	s_barrier
	global_load_lds_dwordx4 v246, s[10:11]
	s_add_u32 m0, s12, 0x1e000
	s_nop 0
	global_load_lds_dwordx4 v247, s[10:11]
	s_waitcnt vmcnt(6)
	s_barrier
	s_setprio 1
	v_mfma_f32_16x16x32_f16 v[42:45], v[178:181], v[194:197], v[42:45]
	v_mfma_f32_16x16x32_f16 v[58:61], v[178:181], v[202:205], v[58:61]
	v_mfma_f32_16x16x32_f16 v[66:69], v[178:181], v[210:213], v[66:69]
	v_mfma_f32_16x16x32_f16 v[70:73], v[186:189], v[194:197], v[70:73]
	v_mfma_f32_16x16x32_f16 v[78:81], v[186:189], v[202:205], v[78:81]
	v_mfma_f32_16x16x32_f16 v[82:85], v[186:189], v[210:213], v[82:85]
	v_mfma_f32_16x16x32_f16 v[42:45], v[182:185], v[198:201], v[42:45]
	v_mfma_f32_16x16x32_f16 v[58:61], v[182:185], v[206:209], v[58:61]
	v_mfma_f32_16x16x32_f16 v[66:69], v[182:185], v[214:217], v[66:69]
	v_mfma_f32_16x16x32_f16 v[70:73], v[190:193], v[198:201], v[70:73]
	v_mfma_f32_16x16x32_f16 v[78:81], v[190:193], v[206:209], v[78:81]
	v_mfma_f32_16x16x32_f16 v[82:85], v[190:193], v[214:217], v[82:85]
	s_setprio 0
	s_add_i32 s2, s2, 2
	s_add_u32 s0, s0, 0x100
	s_addc_u32 s1, s1, 0
	s_add_u32 s8, s8, 0x100
	s_addc_u32 s9, s9, 0
	s_add_u32 s10, s10, 0x100
	s_addc_u32 s11, s11, 0
	s_cmp_lt_u32 s2, 8
	s_barrier
	s_cbranch_scc1 .LBB1_66
	v_readlane_b32 s10, v230, 2
	v_readlane_b32 s11, v230, 3
	v_or_b32_e32 v238, v126, v125
	v_add_u32_e32 v238, v238, v121
	v_lshlrev_b32_e32 v232, 1, v238
	v_and_b32_e32 v232, -4, v232
	v_add_u32_e32 v233, 16, v238
	v_lshlrev_b32_e32 v233, 1, v233
	v_and_b32_e32 v233, -4, v233
	v_add_u32_e32 v234, 32, v238
	v_lshlrev_b32_e32 v234, 1, v234
	v_and_b32_e32 v234, -4, v234
	v_add_u32_e32 v235, 0x60, v238
	v_lshlrev_b32_e32 v235, 1, v235
	v_and_b32_e32 v235, -4, v235
	v_add_u32_e32 v236, 0x70, v238
	v_lshlrev_b32_e32 v236, 1, v236
	v_and_b32_e32 v236, -4, v236
	v_add_u32_e32 v237, 0x80, v238
	v_lshlrev_b32_e32 v237, 1, v237
	v_and_b32_e32 v237, -4, v237
	global_load_dword v232, v232, s[48:49]
	global_load_dword v233, v233, s[48:49]
	global_load_dword v234, v234, s[48:49]
	global_load_dword v235, v235, s[48:49]
	global_load_dword v236, v236, s[48:49]
	global_load_dword v237, v237, s[48:49]
	s_mov_b32 s32, 0x2aaaaaab
	v_mul_hi_u32 v239, v107, s32
	v_lshrrev_b32_e32 v239, 4, v239
	v_mul_u32_u24_e32 v239, 0x60, v239
	v_sub_u32_e32 v239, v107, v239
	v_lshrrev_b32_e32 v240, 1, v121
	v_add_u32_e32 v239, v239, v240
	v_lshlrev_b32_e32 v239, 3, v239
	global_load_dwordx2 v[240:241], v239, s[10:11]
	global_load_dwordx2 v[242:243], v239, s[10:11] offset:3072
	s_mov_b64 s[2:3], 0x580
	v_readfirstlane_b32 s0, v145
	v_lshl_add_u64 v[100:101], v[100:101], 0, s[2:3]
	s_mov_b32 m0, s0
	v_readfirstlane_b32 s0, v146
	ds_read_b128 v[110:113], v144
	ds_read_b128 v[114:117], v144 offset:1024
	ds_read_b128 v[138:141], v144 offset:2048
	ds_read_b128 v[148:151], v144 offset:3072
	ds_read_b128 v[152:155], v144 offset:4096
	ds_read_b128 v[156:159], v144 offset:5120
	ds_read_b128 v[160:163], v130
	ds_read_b128 v[164:167], v130 offset:1024
	ds_read_b128 v[174:177], v108
	ds_read_b128 v[178:181], v108 offset:1024
	global_load_lds_dwordx4 v[100:101], off
	v_lshl_add_u64 v[100:101], v[102:103], 0, s[2:3]
	s_mov_b32 m0, s0
	s_nop 0
	global_load_lds_dwordx4 v[100:101], off
	s_barrier
	s_waitcnt lgkmcnt(0)
	s_setprio 1
	s_waitcnt lgkmcnt(0)
	v_mfma_f32_16x16x32_f16 v[94:97], v[160:163], v[110:113], v[94:97]
	v_mfma_f32_16x16x32_f16 v[90:93], v[160:163], v[138:141], v[90:93]
	v_mfma_f32_16x16x32_f16 v[86:89], v[160:163], v[152:155], v[86:89]
	v_mfma_f32_16x16x32_f16 v[74:77], v[174:177], v[110:113], v[74:77]
	v_mfma_f32_16x16x32_f16 v[18:21], v[174:177], v[152:155], v[18:21]
	v_mfma_f32_16x16x32_f16 v[94:97], v[164:167], v[114:117], v[94:97]
	v_mfma_f32_16x16x32_f16 v[90:93], v[164:167], v[148:151], v[90:93]
	v_mfma_f32_16x16x32_f16 v[86:89], v[164:167], v[156:159], v[86:89]
	v_mfma_f32_16x16x32_f16 v[74:77], v[178:181], v[114:117], v[74:77]
	v_mfma_f32_16x16x32_f16 v[46:49], v[174:177], v[138:141], v[46:49]
	v_mfma_f32_16x16x32_f16 v[18:21], v[178:181], v[156:159], v[18:21]
	v_mfma_f32_16x16x32_f16 v[100:103], v[178:181], v[148:151], v[46:49]
	s_setprio 0
	s_barrier
	s_nop 3
	ds_read_b128 v[46:49], v143
	ds_read_b128 v[144:147], v143 offset:1024
	ds_read_b128 v[182:185], v143 offset:2048
	ds_read_b128 v[186:189], v143 offset:3072
	ds_read_b128 v[190:193], v143 offset:4096
	ds_read_b128 v[194:197], v143 offset:5120
	s_barrier
	s_waitcnt lgkmcnt(0)
	s_setprio 1
	s_waitcnt lgkmcnt(0)
	v_mfma_f32_16x16x32_f16 v[34:37], v[174:177], v[182:185], v[34:37]
	v_mfma_f32_16x16x32_f16 v[10:13], v[160:163], v[46:49], v[10:13]
	v_mfma_f32_16x16x32_f16 v[6:9], v[160:163], v[182:185], v[6:9]
	v_mfma_f32_16x16x32_f16 v[2:5], v[160:163], v[190:193], v[2:5]
	v_mfma_f32_16x16x32_f16 v[26:29], v[174:177], v[46:49], v[26:29]
	v_mfma_f32_16x16x32_f16 v[160:163], v[178:181], v[186:189], v[34:37]
	v_mfma_f32_16x16x32_f16 v[34:37], v[174:177], v[190:193], v[50:53]
	v_mfma_f32_16x16x32_f16 v[10:13], v[164:167], v[144:147], v[10:13]
	v_mfma_f32_16x16x32_f16 v[6:9], v[164:167], v[186:189], v[6:9]
	v_mfma_f32_16x16x32_f16 v[2:5], v[164:167], v[194:197], v[2:5]
	v_mfma_f32_16x16x32_f16 v[26:29], v[178:181], v[144:147], v[26:29]
	v_mfma_f32_16x16x32_f16 v[50:53], v[178:181], v[194:197], v[34:37]
	s_setprio 0
	s_barrier
	s_nop 0
	ds_read_b128 v[34:37], v130 offset:16384
	ds_read_b128 v[164:167], v130 offset:17408
	ds_read_b128 v[174:177], v108 offset:16384
	ds_read_b128 v[178:181], v108 offset:17408
	s_waitcnt vmcnt(12)
	s_barrier
	s_waitcnt lgkmcnt(0)
	s_setprio 1
	s_waitcnt lgkmcnt(0)
	v_mfma_f32_16x16x32_f16 v[22:25], v[34:37], v[138:141], v[22:25]
	v_mfma_f32_16x16x32_f16 v[198:201], v[164:167], v[148:151], v[22:25]
	v_mfma_f32_16x16x32_f16 v[22:25], v[34:37], v[152:155], v[30:33]
	v_mfma_f32_16x16x32_f16 v[30:33], v[164:167], v[156:159], v[22:25]
	v_mfma_f32_16x16x32_f16 v[22:25], v[174:177], v[110:113], v[38:41]
	v_mfma_f32_16x16x32_f16 v[14:17], v[34:37], v[110:113], v[14:17]
	v_mfma_f32_16x16x32_f16 v[110:113], v[178:181], v[114:117], v[22:25]
	v_mfma_f32_16x16x32_f16 v[22:25], v[174:177], v[138:141], v[54:57]
	v_mfma_f32_16x16x32_f16 v[14:17], v[164:167], v[114:117], v[14:17]
	v_mfma_f32_16x16x32_f16 v[54:57], v[178:181], v[148:151], v[22:25]
	v_mfma_f32_16x16x32_f16 v[22:25], v[174:177], v[152:155], v[62:65]
	v_mfma_f32_16x16x32_f16 v[114:117], v[178:181], v[156:159], v[22:25]
	s_setprio 0
	s_setprio 1
	v_mfma_f32_16x16x32_f16 v[22:25], v[34:37], v[46:49], v[42:45]
	v_mfma_f32_16x16x32_f16 v[138:141], v[164:167], v[144:147], v[22:25]
	v_mfma_f32_16x16x32_f16 v[22:25], v[34:37], v[182:185], v[58:61]
	v_mfma_f32_16x16x32_f16 v[148:151], v[164:167], v[186:189], v[22:25]
	v_mfma_f32_16x16x32_f16 v[22:25], v[34:37], v[190:193], v[66:69]
	v_mfma_f32_16x16x32_f16 v[152:155], v[164:167], v[194:197], v[22:25]
	v_mfma_f32_16x16x32_f16 v[22:25], v[174:177], v[46:49], v[70:73]
	v_mfma_f32_16x16x32_f16 v[142:145], v[178:181], v[144:147], v[22:25]
	v_mfma_f32_16x16x32_f16 v[22:25], v[174:177], v[182:185], v[78:81]
	v_mfma_f32_16x16x32_f16 v[156:159], v[178:181], v[186:189], v[22:25]
	v_mfma_f32_16x16x32_f16 v[22:25], v[174:177], v[190:193], v[82:85]
	v_mfma_f32_16x16x32_f16 v[164:167], v[178:181], v[194:197], v[22:25]
	s_setprio 0
	s_barrier
	ds_read_b128 v[58:61], v136
	ds_read_b128 v[174:177], v136 offset:1024
	ds_read_b128 v[178:181], v136 offset:2048
	ds_read_b128 v[182:185], v136 offset:3072
	ds_read_b128 v[186:189], v136 offset:4096
	ds_read_b128 v[134:137], v136 offset:5120
	ds_read_b128 v[34:37], v130 offset:32768
	ds_read_b128 v[62:65], v130 offset:33792
	ds_read_b128 v[78:81], v108 offset:32768
	ds_read_b128 v[190:193], v108 offset:33792
	s_waitcnt vmcnt(2)
	s_barrier
	s_waitcnt lgkmcnt(0)
	s_setprio 1
	s_waitcnt lgkmcnt(0)
	v_mfma_f32_16x16x32_f16 v[22:25], v[34:37], v[58:61], v[94:97]
	v_mfma_f32_16x16x32_f16 v[82:85], v[62:65], v[174:177], v[22:25]
	v_mfma_f32_16x16x32_f16 v[22:25], v[34:37], v[178:181], v[90:93]
	v_mfma_f32_16x16x32_f16 v[70:73], v[62:65], v[182:185], v[22:25]
	v_mfma_f32_16x16x32_f16 v[22:25], v[34:37], v[186:189], v[86:89]
	v_mfma_f32_16x16x32_f16 v[46:49], v[62:65], v[134:137], v[22:25]
	v_mfma_f32_16x16x32_f16 v[22:25], v[78:81], v[58:61], v[74:77]
	v_mfma_f32_16x16x32_f16 v[86:89], v[190:193], v[174:177], v[22:25]
	v_mfma_f32_16x16x32_f16 v[22:25], v[78:81], v[178:181], v[100:103]
	v_mfma_f32_16x16x32_f16 v[18:21], v[78:81], v[186:189], v[18:21]
	v_mfma_f32_16x16x32_f16 v[66:69], v[190:193], v[182:185], v[22:25]
	v_mfma_f32_16x16x32_f16 v[42:45], v[190:193], v[134:137], v[18:21]
	s_setprio 0
	s_barrier
	ds_read_b128 v[100:103], v133
	ds_read_b128 v[194:197], v133 offset:1024
	ds_read_b128 v[202:205], v133 offset:2048
	ds_read_b128 v[206:209], v133 offset:3072
	ds_read_b128 v[210:213], v133 offset:4096
	ds_read_b128 v[214:217], v133 offset:5120
	s_waitcnt vmcnt(0)
	s_barrier
	s_waitcnt lgkmcnt(0)
	s_setprio 1
	s_waitcnt lgkmcnt(0)
	v_mfma_f32_16x16x32_f16 v[6:9], v[34:37], v[202:205], v[6:9]
	v_mfma_f32_16x16x32_f16 v[2:5], v[34:37], v[210:213], v[2:5]
	v_mfma_f32_16x16x32_f16 v[22:25], v[62:65], v[206:209], v[6:9]
	v_mfma_f32_16x16x32_f16 v[6:9], v[62:65], v[214:217], v[2:5]
	v_mfma_f32_16x16x32_f16 v[2:5], v[78:81], v[100:103], v[26:29]
	v_mfma_f32_16x16x32_f16 v[10:13], v[34:37], v[100:103], v[10:13]
	v_mfma_f32_16x16x32_f16 v[34:37], v[190:193], v[194:197], v[2:5]
	v_mfma_f32_16x16x32_f16 v[2:5], v[78:81], v[202:205], v[160:163]
	v_mfma_f32_16x16x32_f16 v[18:21], v[190:193], v[206:209], v[2:5]
	v_mfma_f32_16x16x32_f16 v[2:5], v[78:81], v[210:213], v[50:53]
	v_mfma_f32_16x16x32_f16 v[38:41], v[62:65], v[194:197], v[10:13]
	v_mfma_f32_16x16x32_f16 v[2:5], v[190:193], v[214:217], v[2:5]
	s_setprio 0
	s_barrier
	ds_read_b128 v[10:13], v130 offset:49152
	ds_read_b128 v[26:29], v130 offset:50176
	ds_read_b128 v[128:131], v108 offset:49152
	ds_read_b128 v[160:163], v108 offset:50176
	s_barrier
	s_waitcnt lgkmcnt(0)
	s_setprio 1
	s_waitcnt lgkmcnt(0)
	v_mfma_f32_16x16x32_f16 v[14:17], v[10:13], v[58:61], v[14:17]
	v_mfma_f32_16x16x32_f16 v[90:93], v[26:29], v[174:177], v[14:17]
	v_mfma_f32_16x16x32_f16 v[14:17], v[10:13], v[178:181], v[198:201]
	v_mfma_f32_16x16x32_f16 v[78:81], v[26:29], v[182:185], v[14:17]
	v_mfma_f32_16x16x32_f16 v[14:17], v[10:13], v[186:189], v[30:33]
	v_mfma_f32_16x16x32_f16 v[62:65], v[26:29], v[134:137], v[14:17]
	v_mfma_f32_16x16x32_f16 v[14:17], v[128:131], v[58:61], v[110:113]
	v_mfma_f32_16x16x32_f16 v[94:97], v[160:163], v[174:177], v[14:17]
	v_mfma_f32_16x16x32_f16 v[14:17], v[128:131], v[178:181], v[54:57]
	v_mfma_f32_16x16x32_f16 v[74:77], v[160:163], v[182:185], v[14:17]
	v_mfma_f32_16x16x32_f16 v[14:17], v[128:131], v[186:189], v[114:117]
	v_mfma_f32_16x16x32_f16 v[58:61], v[160:163], v[134:137], v[14:17]
	s_setprio 0
	s_setprio 1
	v_mfma_f32_16x16x32_f16 v[14:17], v[10:13], v[100:103], v[138:141]
	v_mfma_f32_16x16x32_f16 v[54:57], v[26:29], v[194:197], v[14:17]
	v_mfma_f32_16x16x32_f16 v[14:17], v[10:13], v[202:205], v[148:151]
	v_mfma_f32_16x16x32_f16 v[10:13], v[10:13], v[210:213], v[152:155]
	v_mfma_f32_16x16x32_f16 v[30:33], v[26:29], v[206:209], v[14:17]
	v_mfma_f32_16x16x32_f16 v[14:17], v[26:29], v[214:217], v[10:13]
	v_mfma_f32_16x16x32_f16 v[10:13], v[128:131], v[100:103], v[142:145]
	v_mfma_f32_16x16x32_f16 v[50:53], v[160:163], v[194:197], v[10:13]
	v_mfma_f32_16x16x32_f16 v[10:13], v[128:131], v[202:205], v[156:159]
	v_mfma_f32_16x16x32_f16 v[26:29], v[160:163], v[206:209], v[10:13]
	v_mfma_f32_16x16x32_f16 v[10:13], v[128:131], v[210:213], v[164:167]
	v_mfma_f32_16x16x32_f16 v[10:13], v[160:163], v[214:217], v[10:13]
	s_setprio 0
	s_movk_i32 s0, 0x100
	v_cmp_gt_u32_e64 s[0:1], s0, v107
	s_barrier
	s_and_saveexec_b64 s[2:3], s[0:1]
	s_cbranch_execz .LBB1_69
	s_barrier
